# attention task loop: one static s_setprio 1 for waves 0-3 (reset at loop exit); GEMM flips unchanged
# baseline (speedup 1.0000x reference)
; __device__ __forceinline__ void ph_attn(const Frame& F, int j) {
;     ...
;     const float* rpb = inp(F, 10) + (size_t)j * 8 * 465;
;     const int g = F.lane >> 4, l15 = F.lane & 15;
;     const int NLAT = NBAT * 8 * 32, NTASK = NLAT + NBAT * 8;
;     const int wgs = ((F.G & 7) == 0) ? (F.wg & 7) * (F.G >> 3) + (F.wg >> 3) : F.wg;
;     int cidx[4][4];
;     { const int wq_ = (F.wave & 3) * 16 + l15, c0_ = min(max(wq_ - 8, 0), 48);
; #pragma unroll
;       for (int kb = 0; kb < 4; ++kb)
; #pragma unroll
;           for (int i = 0; i < 4; ++i) { const int kc = kb * 16 + 4 * g + i; cidx[kb][i] = (kc >= c0_ && kc < c0_ + 16) ? (kc - wq_ + 15) : 31; } }
;     for (int task = wgs; task < NTASK; task += F.G) {
;         const bool lat = task < NLAT;
;         int b, h, rp4 = 0;
;         if (lat) { b = task >> 8; h = (task >> 5) & 7; rp4 = task & 31; } else { const int t2 = task - NLAT; b = t2 >> 3; h = t2 & 7; }
;         const int w0 = (F.wave & 3) * 16, myr0 = 4 * rp4 + 2 * (F.wave >> 2);
;         const int rlo = min(max(4 * rp4 - 4, 0), 120), rhi = min(max(4 * rp4 + 3 - 4, 0), 120) + 7;
;         const int nloc = lat ? (rhi - rlo + 1) : 0;
;         int qrow[2], r0t[2];
;         bf16x8 qf[2][2];
; #pragma unroll
;         for (int T = 0; T < 2; ++T) { r0t[T] = min(max(myr0 + T - 4, 0), 120);
;             qrow[T] = lat ? (TC + b * SEQ + (myr0 + T) * 64 + w0 + l15) : (b * CTXL + (2 * F.wave + T) * 16 + l15);
;             qf[T][0] = *(const bf16x8*)(P + (size_t)qrow[T] * 4096 + h * 64 + g * 8);
;             qf[T][1] = *(const bf16x8*)(P + (size_t)qrow[T] * 4096 + h * 64 + 32 + g * 8); }
;         if (lat) for (int i = F.tid; i < 480; i += 512) { const int rr = i >> 5, cc = i & 31; rp_l[i] = (cc < 31) ? rpb[h * 465 + rr * 31 + cc] * 1.4426950408889634f : -1e30f; }
.LBB0_473:
	s_and_b64 vcc, exec, s[0:1]
	s_cbranch_vccz .LBB0_699
	v_readlane_b32 s0, v251, 10
	v_readlane_b32 s1, v251, 11
	s_andn2_b64 vcc, exec, s[0:1]
	s_mov_b64 s[0:1], -1
	s_cbranch_vccnz .LBB0_669
	v_readlane_b32 s0, v254, 39
	v_mov_b32_e32 v0, v177
	s_mov_b32 s14, s26
	v_mov_b32_e32 v1, s0
	s_waitcnt vmcnt(0)
	ds_read_b64 v[4:5], v1
	v_readlane_b32 s0, v253, 7
	v_readlane_b32 s1, v253, 8
	s_and_b64 vcc, exec, s[0:1]
	s_waitcnt lgkmcnt(0)
	v_readfirstlane_b32 s0, v5
	v_readfirstlane_b32 s1, v4
	s_cbranch_vccz .LBB0_668
	s_mul_i32 s2, s14, 0x3a20
	s_add_u32 s58, s1, s2
	s_addc_u32 s59, s0, 0
	v_and_b32_e32 v158, 15, v0
	v_readlane_b32 s0, v253, 9
	v_ashrrev_i32_e32 v1, 4, v0
	v_add_u32_e32 v145, s79, v0
	v_or_b32_e32 v3, s0, v158
	v_sub_u32_e64 v4, v3, 8 clamp
	v_min_u32_e32 v5, 48, v4
	v_lshlrev_b32_e32 v4, 2, v1
	v_add_u32_e32 v6, 16, v5
	v_cmp_ge_i32_e32 vcc, v4, v5
	v_cmp_lt_i32_e64 s[42:43], v4, v6
	v_sub_u32_e32 v7, v4, v3
	v_add_u32_e32 v8, 15, v7
	s_and_b64 vcc, vcc, s[42:43]
	v_cndmask_b32_e32 v159, 31, v8, vcc
	v_or_b32_e32 v8, 1, v4
	v_cmp_ge_i32_e32 vcc, v8, v5
	v_cmp_lt_i32_e64 s[42:43], v8, v6
	v_sub_u32_e32 v8, v8, v3
	v_add_u32_e32 v8, 15, v8
	s_and_b64 vcc, vcc, s[42:43]
	v_cndmask_b32_e32 v160, 31, v8, vcc
	v_or_b32_e32 v8, 2, v4
	v_cmp_ge_i32_e32 vcc, v8, v5
	v_cmp_lt_i32_e64 s[42:43], v8, v6
	v_sub_u32_e32 v8, v8, v3
	v_add_u32_e32 v8, 15, v8
	s_and_b64 vcc, vcc, s[42:43]
	v_cndmask_b32_e32 v161, 31, v8, vcc
	v_or_b32_e32 v8, 3, v4
	v_cmp_ge_i32_e32 vcc, v8, v5
	v_cmp_lt_i32_e64 s[42:43], v8, v6
	v_sub_u32_e32 v3, v8, v3
	v_add_u32_e32 v3, 15, v3
	s_and_b64 vcc, vcc, s[42:43]
	v_cndmask_b32_e32 v162, 31, v3, vcc
	v_add_u32_e32 v3, 16, v4
	v_cmp_ge_i32_e32 vcc, v3, v5
	v_cmp_lt_i32_e64 s[42:43], v4, v5
	v_add_u32_e32 v3, 31, v7
	s_and_b64 vcc, vcc, s[42:43]
	v_cndmask_b32_e32 v163, 31, v3, vcc
	v_add_u32_e32 v3, 17, v4
	v_cmp_ge_i32_e32 vcc, v3, v5
	v_cmp_lt_i32_e64 s[42:43], v3, v6
	v_add_u32_e32 v3, 32, v7
	s_and_b64 vcc, vcc, s[42:43]
	v_cndmask_b32_e32 v164, 31, v3, vcc
	v_add_u32_e32 v3, 18, v4
	v_cmp_ge_i32_e32 vcc, v3, v5
	v_cmp_lt_i32_e64 s[42:43], v3, v6
	v_add_u32_e32 v3, 33, v7
	s_and_b64 vcc, vcc, s[42:43]
	v_cndmask_b32_e32 v165, 31, v3, vcc
	v_add_u32_e32 v3, 19, v4
	v_cmp_ge_i32_e32 vcc, v3, v5
	v_cmp_lt_i32_e64 s[42:43], v3, v6
	v_add_u32_e32 v3, 34, v7
	s_and_b64 vcc, vcc, s[42:43]
	v_cndmask_b32_e32 v166, 31, v3, vcc
	v_add_u32_e32 v3, 32, v4
	v_cmp_ge_i32_e32 vcc, v3, v5
	v_cmp_lt_i32_e64 s[42:43], v3, v6
	v_add_u32_e32 v8, 47, v7
	s_and_b64 vcc, vcc, s[42:43]
	v_cndmask_b32_e32 v167, 31, v8, vcc
	v_add_u32_e32 v8, 33, v4
	v_cmp_ge_i32_e32 vcc, v8, v5
	v_cmp_lt_i32_e64 s[42:43], v8, v6
	v_add_u32_e32 v8, 48, v7
	s_and_b64 vcc, vcc, s[42:43]
	v_cndmask_b32_e32 v168, 31, v8, vcc
	v_add_u32_e32 v8, 34, v4
	v_cmp_ge_i32_e32 vcc, v8, v5
	v_cmp_lt_i32_e64 s[42:43], v8, v6
	v_add_u32_e32 v8, 49, v7
	s_and_b64 vcc, vcc, s[42:43]
	v_cndmask_b32_e32 v169, 31, v8, vcc
	v_add_u32_e32 v8, 35, v4
	v_cmp_ge_i32_e32 vcc, v8, v5
	v_cmp_lt_i32_e64 s[42:43], v8, v6
	v_add_u32_e32 v8, 50, v7
	s_and_b64 vcc, vcc, s[42:43]
	v_cndmask_b32_e32 v170, 31, v8, vcc
	v_add_u32_e32 v8, 48, v4
	v_cmp_ge_i32_e32 vcc, v8, v5
	v_cmp_lt_i32_e64 s[42:43], v8, v6
	v_add_u32_e32 v8, 63, v7
	s_and_b64 vcc, vcc, s[42:43]
	v_cndmask_b32_e32 v171, 31, v8, vcc
	v_add_u32_e32 v8, 49, v4
	v_cmp_ge_i32_e32 vcc, v8, v5
	v_cmp_lt_i32_e64 s[42:43], v8, v6
	v_add_u32_e32 v8, 64, v7
	s_and_b64 vcc, vcc, s[42:43]
	v_cndmask_b32_e32 v172, 31, v8, vcc
	v_add_u32_e32 v8, 50, v4
	v_cmp_ge_i32_e32 vcc, v8, v5
	v_cmp_lt_i32_e64 s[42:43], v8, v6
	v_add_u32_e32 v8, 0x41, v7
	s_and_b64 vcc, vcc, s[42:43]
	v_cndmask_b32_e32 v173, 31, v8, vcc
	v_add_u32_e32 v8, 51, v4
	v_cmp_ge_i32_e32 vcc, v8, v5
	v_cmp_lt_i32_e64 s[42:43], v8, v6
	v_add_u32_e32 v5, 0x42, v7
	s_and_b64 vcc, vcc, s[42:43]
	v_cndmask_b32_e32 v190, 31, v5, vcc
	v_lshlrev_b32_e32 v6, 3, v1
	v_and_b32_e32 v1, -16, v0
	v_mul_u32_u24_e32 v5, 0x90, v158
	v_add3_u32 v191, 0, v1, v5
	v_bfe_u32 v1, v0, 2, 2
	v_or_b32_e32 v5, v4, v1
	s_movk_i32 s1, 0x90
	v_lshlrev_b32_e32 v8, 3, v0
	v_or_b32_e32 v1, v3, v1
	v_mul_lo_u32 v5, v5, s1
	v_and_b32_e32 v9, 24, v8
	v_mul_lo_u32 v1, v1, s1
	s_movk_i32 s0, 0x1e0
	v_ashrrev_i32_e32 v194, 3, v145
	v_and_b32_e32 v8, 56, v8
	v_ashrrev_i32_e32 v7, 31, v6
	v_add3_u32 v192, 0, v5, v9
	v_add3_u32 v193, 0, v1, v9
	v_ashrrev_i32_e32 v5, 31, v4
	v_cmp_gt_i32_e64 s[42:43], s0, v145
	v_lshlrev_b32_e32 v10, 1, v8
	v_and_b32_e32 v195, 31, v0
	v_mul_lo_u32 v1, v194, s1
	v_mov_b32_e32 v11, v2
	v_readlane_b32 s0, v253, 32
	v_cmp_ne_u32_e64 s[44:45], 31, v195
	v_add3_u32 v196, 0, v10, v1
	v_lshl_add_u64 v[116:117], s[82:83], 0, v[10:11]
	v_lshl_add_u32 v197, v0, 2, s0
	v_lshlrev_b32_e32 v198, 2, v159
	v_lshlrev_b32_e32 v199, 2, v160
	v_lshlrev_b32_e32 v200, 2, v161
	v_lshlrev_b32_e32 v201, 2, v162
	v_lshlrev_b32_e32 v202, 2, v163
	v_lshlrev_b32_e32 v203, 2, v164
	v_lshlrev_b32_e32 v204, 2, v165
	v_lshlrev_b32_e32 v205, 2, v166
	v_lshlrev_b32_e32 v206, 2, v167
	v_lshlrev_b32_e32 v207, 2, v168
	v_lshlrev_b32_e32 v208, 2, v169
	v_lshlrev_b32_e32 v209, 2, v170
	v_lshlrev_b32_e32 v210, 2, v171
	v_lshlrev_b32_e32 v211, 2, v172
	v_lshlrev_b32_e32 v212, 2, v173
	v_lshlrev_b32_e32 v213, 2, v190
	v_lshlrev_b64 v[118:119], 1, v[6:7]
	v_lshlrev_b32_e32 v120, 1, v8
	v_lshlrev_b64 v[122:123], 1, v[4:5]
	v_readlane_b32 s8, v253, 6
	s_cmp_ge_u32 s75, 4
	s_cbranch_scc1 .Lattn_prio_skip
	s_setprio 1
.Lattn_prio_skip:
	s_branch .LBB0_479

; __device__ __forceinline__ void ph_attn(const Frame& F, int j) {
;     ...
;     for (int task = wgs; task < NTASK; task += F.G) {
;     ...
;     }
; }
.LBB0_668:
	s_setprio 0
	s_mov_b64 s[0:1], 0
	s_mov_b32 s26, s14
